# P8 leftover-quantizer loops: pipelined ticket draw (thread 0 no longer drains vmcnt + waits for the atomic at the top of every item); on top of v70
# baseline (speedup 1.0000x reference)
; #define Q_LOAD() do { _Pragma("unroll") for (int g = 0; g < 8; ++g) _Pragma("unroll") for (int r = 0; r < 4; ++r) v[g][r] = __builtin_nontemporal_load((const f32x4*)(Wp + (size_t)(256 * g + 32 * wave + 4 * kr + r) * ldw + 4 * n4)); } while (0)
; #define Q_GRAB() (((stop != nullptr && xb_ld(stop) >= thr) || (quota > 0 && qleft-- <= 0)) ? (unsigned)hi : (unsigned)lo + atomicAdd(cnt, 1u))
;     ...
;     __syncthreads();
;     if (tid == 0) MISC[2] = Q_GRAB();
;     __syncthreads();
;     int cur = (int)MISC[2];
;     __syncthreads();
;     if (cur < hi) { Q_ITEM(cur); Q_LOAD(); }
;     while (cur < hi) {
;         unsigned nxt = 0u; if (tid == 0) nxt = Q_GRAB();
.LBB0_1722:
	s_or_b64 exec, exec, s[6:7]
	s_waitcnt vmcnt(0)
	v_readfirstlane_b32 s7, v2
	s_add_i32 s6, s10, -1
	v_mov_b32_e32 v163, s6
	v_add_u32_e32 v1, s7, v1
	s_add_i32 s7, 0, 0x27f08
	v_add_u32_e32 v1, 0x1c8, v1
	v_mov_b32_e32 v2, s7
	ds_write_b32 v2, v1
	v_mov_b32_e32 v201, 0x1800
	v_cmp_lt_i32_e32 vcc, 0, v163
	s_mov_b64 s[8:9], exec
	s_and_b64 exec, exec, vcc
	v_mov_b32_e32 v203, 1
	v_mov_b32_e32 v2, 0
	global_atomic_add v201, v2, v203, s[20:21] sc0
	s_mov_b64 exec, s[8:9]
	v_add_u32_e32 v163, -1, v163

; #define LAS __attribute__((address_space(3)))
; #define Q_GRAB() (((stop != nullptr && xb_ld(stop) >= thr) || (quota > 0 && qleft-- <= 0)) ? (unsigned)hi : (unsigned)lo + atomicAdd(cnt, 1u))
;     ...
;     while (cur < hi) {
;         unsigned nxt = 0u; if (tid == 0) nxt = Q_GRAB();
;         signed char* Qc = Qp; float* csc = csp; const bool f8c = f8; const float qmax = f8c ? 448.0f : 127.0f, qinv = f8c ? (1.0f / 448.0f) : (1.0f / 127.0f);
;         f32x4 mx = {0.f, 0.f, 0.f, 0.f};
; #pragma unroll
;         for (int g = 0; g < 8; ++g)
; #pragma unroll
;             for (int r = 0; r < 4; ++r) { mx[0] = fmaxf(mx[0], fabsf(v[g][r][0])); mx[1] = fmaxf(mx[1], fabsf(v[g][r][1])); mx[2] = fmaxf(mx[2], fabsf(v[g][r][2])); mx[3] = fmaxf(mx[3], fabsf(v[g][r][3])); }
; #pragma unroll
;         for (int c = 0; c < 4; ++c) { float m = mx[c]; m = fmaxf(m, __shfl_xor(m, 8)); m = fmaxf(m, __shfl_xor(m, 16)); m = fmaxf(m, __shfl_xor(m, 32)); mx[c] = m; }
;         if (tid == 0) MISC[2] = nxt;
;         if (kr == 0) *(LAS f32x4*)(smax + wave * 32 + 4 * n4) = mx;
;         __syncthreads();
;         const int nx = (int)MISC[2]; const bool more = nx < hi;
;         f32x4 cm = *(const LAS f32x4*)(smax + 4 * n4);
; #pragma unroll
;         for (int ww = 1; ww < 8; ++ww) { const f32x4 o = *(const LAS f32x4*)(smax + ww * 32 + 4 * n4); cm[0] = fmaxf(cm[0], o[0]); cm[1] = fmaxf(cm[1], o[1]); cm[2] = fmaxf(cm[2], o[2]); cm[3] = fmaxf(cm[3], o[3]); }
.LBB0_1748:
	s_waitcnt vmcnt(10)
	v_max3_f32 v130, |v2|, 0, |v6|
	s_waitcnt vmcnt(8)
	v_max3_f32 v130, v130, |v10|, |v14|
	s_waitcnt vmcnt(26)
	v_max3_f32 v130, v130, |v18|, |v22|
	s_waitcnt vmcnt(24)
	v_max3_f32 v130, v130, |v26|, |v30|
	s_waitcnt vmcnt(22)
	v_max3_f32 v130, v130, |v34|, |v38|
	s_waitcnt vmcnt(20)
	v_max3_f32 v130, v130, |v42|, |v46|
	v_max3_f32 v131, |v3|, 0, |v7|
	s_waitcnt vmcnt(18)
	v_max3_f32 v130, v130, |v50|, |v54|
	v_max3_f32 v132, |v4|, 0, |v8|
	v_max3_f32 v131, v131, |v11|, |v15|
	s_waitcnt vmcnt(16)
	v_max3_f32 v130, v130, |v58|, |v62|
	v_max3_f32 v132, v132, |v12|, |v16|
	v_max3_f32 v131, v131, |v19|, |v23|
	s_waitcnt vmcnt(14)
	v_max3_f32 v130, v130, |v66|, |v70|
	v_max3_f32 v132, v132, |v20|, |v24|
	v_max3_f32 v131, v131, |v27|, |v31|
	s_waitcnt vmcnt(12)
	v_max3_f32 v130, v130, |v74|, |v78|
	v_max3_f32 v132, v132, |v28|, |v32|
	v_max3_f32 v131, v131, |v35|, |v39|
	s_waitcnt vmcnt(10)
	v_max3_f32 v130, v130, |v82|, |v86|
	v_max3_f32 v132, v132, |v36|, |v40|
	v_max3_f32 v131, v131, |v43|, |v47|
	s_waitcnt vmcnt(8)
	v_max3_f32 v130, v130, |v90|, |v94|
	v_max3_f32 v132, v132, |v44|, |v48|
	v_max3_f32 v131, v131, |v51|, |v55|
	s_waitcnt vmcnt(6)
	v_max3_f32 v130, v130, |v98|, |v102|
	v_max3_f32 v133, |v5|, 0, |v9|
	v_max3_f32 v132, v132, |v52|, |v56|
	v_max3_f32 v131, v131, |v59|, |v63|
	s_waitcnt vmcnt(4)
	v_max3_f32 v130, v130, |v106|, |v110|
	v_max3_f32 v133, v133, |v13|, |v17|
	v_max3_f32 v132, v132, |v60|, |v64|
	v_max3_f32 v131, v131, |v67|, |v71|
	s_waitcnt vmcnt(2)
	v_max3_f32 v130, v130, |v114|, |v118|
	v_max3_f32 v133, v133, |v21|, |v25|
	v_max3_f32 v132, v132, |v68|, |v72|
	v_max3_f32 v131, v131, |v75|, |v79|
	s_waitcnt vmcnt(0)
	v_max3_f32 v130, v130, |v122|, |v126|
	v_max3_f32 v133, v133, |v29|, |v33|
	v_max3_f32 v132, v132, |v76|, |v80|
	v_max3_f32 v131, v131, |v83|, |v87|
	ds_bpermute_b32 v134, v165, v130
	v_max3_f32 v133, v133, |v37|, |v41|
	v_max3_f32 v132, v132, |v84|, |v88|
	v_max3_f32 v131, v131, |v91|, |v95|
	v_max3_f32 v133, v133, |v45|, |v49|
	v_max3_f32 v132, v132, |v92|, |v96|
	v_max3_f32 v131, v131, |v99|, |v103|
	v_max3_f32 v133, v133, |v53|, |v57|
	v_max3_f32 v132, v132, |v100|, |v104|
	v_max3_f32 v131, v131, |v107|, |v111|
	v_max3_f32 v133, v133, |v61|, |v65|
	v_max3_f32 v132, v132, |v108|, |v112|
	v_max3_f32 v131, v131, |v115|, |v119|
	v_max3_f32 v133, v133, |v69|, |v73|
	v_max3_f32 v132, v132, |v116|, |v120|
	v_max3_f32 v131, v131, |v123|, |v127|
	s_waitcnt lgkmcnt(0)
	v_max_f32_e32 v134, v134, v134
	v_max3_f32 v133, v133, |v77|, |v81|
	v_max3_f32 v135, v132, |v124|, |v128|
	ds_bpermute_b32 v132, v165, v131
	v_max_f32_e32 v130, v130, v134
	v_max3_f32 v133, v133, |v85|, |v89|
	ds_bpermute_b32 v134, v167, v130
	v_max3_f32 v133, v133, |v93|, |v97|
	v_max3_f32 v133, v133, |v101|, |v105|
	v_max3_f32 v133, v133, |v109|, |v113|
	v_max3_f32 v133, v133, |v117|, |v121|
	s_waitcnt lgkmcnt(1)
	v_max_f32_e32 v132, v132, v132
	v_max3_f32 v133, v133, |v125|, |v129|
	v_max_f32_e32 v132, v131, v132
	s_waitcnt lgkmcnt(0)
	v_max_f32_e32 v131, v134, v134
	ds_bpermute_b32 v134, v165, v135
	ds_bpermute_b32 v136, v167, v132
	ds_bpermute_b32 v137, v165, v133
	v_max_f32_e32 v130, v130, v131
	ds_bpermute_b32 v131, v169, v130
	s_waitcnt lgkmcnt(3)
	v_max_f32_e32 v134, v134, v134
	s_waitcnt lgkmcnt(2)
	v_max_f32_e32 v136, v136, v136
	v_max_f32_e32 v134, v135, v134
	s_waitcnt lgkmcnt(1)
	v_max_f32_e32 v135, v137, v137
	v_max_f32_e32 v132, v132, v136
	ds_bpermute_b32 v136, v167, v134
	v_max_f32_e32 v137, v133, v135
	ds_bpermute_b32 v138, v167, v137
	ds_bpermute_b32 v135, v169, v132
	s_waitcnt lgkmcnt(2)
	v_max_f32_e32 v133, v136, v136
	v_max_f32_e32 v133, v134, v133
	s_waitcnt lgkmcnt(1)
	v_max_f32_e32 v134, v138, v138
	v_max_f32_e32 v134, v137, v134
	ds_bpermute_b32 v136, v169, v133
	ds_bpermute_b32 v137, v169, v134
	s_and_saveexec_b64 s[6:7], s[40:41]
	v_add_u32_e32 v1, 0x1c8, v201
	v_cmp_lt_i32_e32 vcc, 0, v163
	v_mov_b32_e32 v201, 0x1800
	s_and_b64 exec, exec, vcc
	v_mov_b32_e32 v203, 1
	global_atomic_add v201, v171, v203, s[20:21] sc0
	s_and_b64 exec, s[6:7], s[40:41]
	v_add_u32_e32 v163, -1, v163
	v_mov_b32_e32 v138, s3
	ds_write_b32 v138, v1
	s_or_b64 exec, exec, s[6:7]
	s_and_saveexec_b64 s[6:7], s[4:5]
	s_cbranch_execz .LBB0_1758
	v_max_f32_e32 v1, v131, v131
	v_max_f32_e32 v130, v130, v130
	v_max_f32_e32 v130, v130, v1
	s_waitcnt lgkmcnt(2)
	v_max_f32_e32 v1, v135, v135
	v_max_f32_e32 v131, v132, v132
	v_max_f32_e32 v131, v131, v1
	s_waitcnt lgkmcnt(1)
	v_max_f32_e32 v1, v136, v136
	v_max_f32_e32 v132, v133, v133
	v_max_f32_e32 v132, v132, v1
	s_waitcnt lgkmcnt(0)
	v_max_f32_e32 v1, v137, v137
	v_max_f32_e32 v133, v134, v134
	v_max_f32_e32 v133, v133, v1
	v_add_u32_e32 v1, s42, v173
	ds_write_b128 v1, v[130:133]

; #define Q_LOAD() do { _Pragma("unroll") for (int g = 0; g < 8; ++g) _Pragma("unroll") for (int r = 0; r < 4; ++r) v[g][r] = __builtin_nontemporal_load((const f32x4*)(Wp + (size_t)(256 * g + 32 * wave + 4 * kr + r) * ldw + 4 * n4)); } while (0)
; #define Q_GRAB() (((stop != nullptr && xb_ld(stop) >= thr) || (quota > 0 && qleft-- <= 0)) ? (unsigned)hi : (unsigned)lo + atomicAdd(cnt, 1u))
;     ...
;     __syncthreads();
;     if (tid == 0) MISC[2] = Q_GRAB();
;     __syncthreads();
;     int cur = (int)MISC[2];
;     __syncthreads();
;     if (cur < hi) { Q_ITEM(cur); Q_LOAD(); }
;     while (cur < hi) {
;         unsigned nxt = 0u; if (tid == 0) nxt = Q_GRAB();
.LBB0_1962:
	s_or_b64 exec, exec, s[6:7]
	s_waitcnt vmcnt(0)
	v_readfirstlane_b32 s3, v2
	s_nop 1
	v_add_u32_e32 v1, s3, v1
	s_add_i32 s3, 0, 0x27f08
	v_add_u32_e32 v1, 0x1c8, v1
	v_mov_b32_e32 v2, s3
	ds_write_b32 v2, v1
	v_mov_b32_e32 v203, 1
	v_mov_b32_e32 v2, 0
	global_atomic_add v199, v2, v203, s[20:21] sc0

; #define LAS __attribute__((address_space(3)))
; #define Q_GRAB() (((stop != nullptr && xb_ld(stop) >= thr) || (quota > 0 && qleft-- <= 0)) ? (unsigned)hi : (unsigned)lo + atomicAdd(cnt, 1u))
;     ...
;     while (cur < hi) {
;         unsigned nxt = 0u; if (tid == 0) nxt = Q_GRAB();
;         signed char* Qc = Qp; float* csc = csp; const bool f8c = f8; const float qmax = f8c ? 448.0f : 127.0f, qinv = f8c ? (1.0f / 448.0f) : (1.0f / 127.0f);
;         f32x4 mx = {0.f, 0.f, 0.f, 0.f};
; #pragma unroll
;         for (int g = 0; g < 8; ++g)
; #pragma unroll
;             for (int r = 0; r < 4; ++r) { mx[0] = fmaxf(mx[0], fabsf(v[g][r][0])); mx[1] = fmaxf(mx[1], fabsf(v[g][r][1])); mx[2] = fmaxf(mx[2], fabsf(v[g][r][2])); mx[3] = fmaxf(mx[3], fabsf(v[g][r][3])); }
; #pragma unroll
;         for (int c = 0; c < 4; ++c) { float m = mx[c]; m = fmaxf(m, __shfl_xor(m, 8)); m = fmaxf(m, __shfl_xor(m, 16)); m = fmaxf(m, __shfl_xor(m, 32)); mx[c] = m; }
;         if (tid == 0) MISC[2] = nxt;
;         if (kr == 0) *(LAS f32x4*)(smax + wave * 32 + 4 * n4) = mx;
;         __syncthreads();
;         const int nx = (int)MISC[2]; const bool more = nx < hi;
;         f32x4 cm = *(const LAS f32x4*)(smax + 4 * n4);
; #pragma unroll
;         for (int ww = 1; ww < 8; ++ww) { const f32x4 o = *(const LAS f32x4*)(smax + ww * 32 + 4 * n4); cm[0] = fmaxf(cm[0], o[0]); cm[1] = fmaxf(cm[1], o[1]); cm[2] = fmaxf(cm[2], o[2]); cm[3] = fmaxf(cm[3], o[3]); }
.LBB0_1987:
	s_waitcnt vmcnt(10)
	v_max3_f32 v130, |v2|, 0, |v6|
	s_waitcnt vmcnt(8)
	v_max3_f32 v130, v130, |v10|, |v14|
	s_waitcnt vmcnt(26)
	v_max3_f32 v130, v130, |v18|, |v22|
	s_waitcnt vmcnt(24)
	v_max3_f32 v130, v130, |v26|, |v30|
	s_waitcnt vmcnt(22)
	v_max3_f32 v130, v130, |v34|, |v38|
	s_waitcnt vmcnt(20)
	v_max3_f32 v130, v130, |v42|, |v46|
	v_max3_f32 v131, |v3|, 0, |v7|
	s_waitcnt vmcnt(18)
	v_max3_f32 v130, v130, |v50|, |v54|
	v_max3_f32 v132, |v4|, 0, |v8|
	v_max3_f32 v131, v131, |v11|, |v15|
	s_waitcnt vmcnt(16)
	v_max3_f32 v130, v130, |v58|, |v62|
	v_max3_f32 v132, v132, |v12|, |v16|
	v_max3_f32 v131, v131, |v19|, |v23|
	s_waitcnt vmcnt(14)
	v_max3_f32 v130, v130, |v66|, |v70|
	v_max3_f32 v132, v132, |v20|, |v24|
	v_max3_f32 v131, v131, |v27|, |v31|
	s_waitcnt vmcnt(12)
	v_max3_f32 v130, v130, |v74|, |v78|
	v_max3_f32 v132, v132, |v28|, |v32|
	v_max3_f32 v131, v131, |v35|, |v39|
	s_waitcnt vmcnt(10)
	v_max3_f32 v130, v130, |v82|, |v86|
	v_max3_f32 v132, v132, |v36|, |v40|
	v_max3_f32 v131, v131, |v43|, |v47|
	s_waitcnt vmcnt(8)
	v_max3_f32 v130, v130, |v90|, |v94|
	v_max3_f32 v132, v132, |v44|, |v48|
	v_max3_f32 v131, v131, |v51|, |v55|
	s_waitcnt vmcnt(6)
	v_max3_f32 v130, v130, |v98|, |v102|
	v_max3_f32 v133, |v5|, 0, |v9|
	v_max3_f32 v132, v132, |v52|, |v56|
	v_max3_f32 v131, v131, |v59|, |v63|
	s_waitcnt vmcnt(4)
	v_max3_f32 v130, v130, |v106|, |v110|
	v_max3_f32 v133, v133, |v13|, |v17|
	v_max3_f32 v132, v132, |v60|, |v64|
	v_max3_f32 v131, v131, |v67|, |v71|
	s_waitcnt vmcnt(2)
	v_max3_f32 v130, v130, |v114|, |v118|
	v_max3_f32 v133, v133, |v21|, |v25|
	v_max3_f32 v132, v132, |v68|, |v72|
	v_max3_f32 v131, v131, |v75|, |v79|
	s_waitcnt vmcnt(0)
	v_max3_f32 v130, v130, |v122|, |v126|
	v_max3_f32 v133, v133, |v29|, |v33|
	v_max3_f32 v132, v132, |v76|, |v80|
	v_max3_f32 v131, v131, |v83|, |v87|
	ds_bpermute_b32 v134, v163, v130
	v_max3_f32 v133, v133, |v37|, |v41|
	v_max3_f32 v132, v132, |v84|, |v88|
	v_max3_f32 v131, v131, |v91|, |v95|
	v_max3_f32 v133, v133, |v45|, |v49|
	v_max3_f32 v132, v132, |v92|, |v96|
	v_max3_f32 v131, v131, |v99|, |v103|
	v_max3_f32 v133, v133, |v53|, |v57|
	v_max3_f32 v132, v132, |v100|, |v104|
	v_max3_f32 v131, v131, |v107|, |v111|
	v_max3_f32 v133, v133, |v61|, |v65|
	v_max3_f32 v132, v132, |v108|, |v112|
	v_max3_f32 v131, v131, |v115|, |v119|
	v_max3_f32 v133, v133, |v69|, |v73|
	v_max3_f32 v132, v132, |v116|, |v120|
	v_max3_f32 v131, v131, |v123|, |v127|
	s_waitcnt lgkmcnt(0)
	v_max_f32_e32 v134, v134, v134
	v_max3_f32 v133, v133, |v77|, |v81|
	v_max3_f32 v135, v132, |v124|, |v128|
	ds_bpermute_b32 v132, v163, v131
	v_max_f32_e32 v130, v130, v134
	v_max3_f32 v133, v133, |v85|, |v89|
	ds_bpermute_b32 v134, v165, v130
	v_max3_f32 v133, v133, |v93|, |v97|
	v_max3_f32 v133, v133, |v101|, |v105|
	v_max3_f32 v133, v133, |v109|, |v113|
	v_max3_f32 v133, v133, |v117|, |v121|
	s_waitcnt lgkmcnt(1)
	v_max_f32_e32 v132, v132, v132
	v_max3_f32 v133, v133, |v125|, |v129|
	v_max_f32_e32 v132, v131, v132
	s_waitcnt lgkmcnt(0)
	v_max_f32_e32 v131, v134, v134
	ds_bpermute_b32 v134, v163, v135
	ds_bpermute_b32 v136, v165, v132
	ds_bpermute_b32 v137, v163, v133
	v_max_f32_e32 v130, v130, v131
	ds_bpermute_b32 v131, v167, v130
	s_waitcnt lgkmcnt(3)
	v_max_f32_e32 v134, v134, v134
	s_waitcnt lgkmcnt(2)
	v_max_f32_e32 v136, v136, v136
	v_max_f32_e32 v134, v135, v134
	s_waitcnt lgkmcnt(1)
	v_max_f32_e32 v135, v137, v137
	v_max_f32_e32 v132, v132, v136
	ds_bpermute_b32 v136, v165, v134
	v_max_f32_e32 v137, v133, v135
	ds_bpermute_b32 v138, v165, v137
	ds_bpermute_b32 v135, v167, v132
	s_waitcnt lgkmcnt(2)
	v_max_f32_e32 v133, v136, v136
	v_max_f32_e32 v133, v134, v133
	s_waitcnt lgkmcnt(1)
	v_max_f32_e32 v134, v138, v138
	v_max_f32_e32 v134, v137, v134
	ds_bpermute_b32 v136, v167, v133
	ds_bpermute_b32 v137, v167, v134
	s_and_saveexec_b64 s[6:7], s[40:41]
	v_add_u32_e32 v1, 0x1c8, v199
	v_mov_b32_e32 v203, 1
	global_atomic_add v199, v171, v203, s[20:21] sc0
	v_mov_b32_e32 v138, s69
	ds_write_b32 v138, v1
	s_or_b64 exec, exec, s[6:7]
	s_and_saveexec_b64 s[6:7], s[4:5]
	s_cbranch_execz .LBB0_1995
	v_max_f32_e32 v1, v131, v131
	v_max_f32_e32 v130, v130, v130
	v_max_f32_e32 v130, v130, v1
	s_waitcnt lgkmcnt(2)
	v_max_f32_e32 v1, v135, v135
	v_max_f32_e32 v131, v132, v132
	v_max_f32_e32 v131, v131, v1
	s_waitcnt lgkmcnt(1)
	v_max_f32_e32 v1, v136, v136
	v_max_f32_e32 v132, v133, v133
	v_max_f32_e32 v132, v132, v1
	s_waitcnt lgkmcnt(0)
	v_max_f32_e32 v1, v137, v137
	v_max_f32_e32 v133, v134, v134
	v_max_f32_e32 v133, v133, v1
	v_add_u32_e32 v1, s38, v169
	ds_write_b128 v1, v[130:133]
